# barrier: flat release - each XCD leader publishes its generation after wbl2, every workgroup polls all 16 XCD flags (no TOP counter / TOPGEN hop); early L1 invalidate
# speedup vs baseline: 1.0015x; 1.0015x over previous
; __device__ __forceinline__ unsigned xb_ld(unsigned* p)              { return __hip_atomic_load(p, __ATOMIC_RELAXED, __HIP_MEMORY_SCOPE_AGENT); }
; __device__ __forceinline__ unsigned xb_add(unsigned* p, unsigned v) { return __hip_atomic_fetch_add(p, v, __ATOMIC_RELAXED, __HIP_MEMORY_SCOPE_AGENT); }
; #define XB_SPIN(cond, bar) do { unsigned _sp = 0; while (cond) { __builtin_amdgcn_s_sleep(1); \
;     if ((++_sp & 255u) == 0u) { if (xb_ld(&(bar)[XB_TMO])) break; if (_sp > XB_SPIN_CAP) { atomicAdd(&(bar)[XB_TMO], 1u); break; } } } } while (0)
; __device__ __forceinline__ void xcd_barrier(const XcdBarrier& b) {
;     asm volatile("s_waitcnt vmcnt(0)" ::: "memory");
;     __syncthreads();
;     int ln_; asm volatile("v_mbcnt_lo_u32_b32 %0, -1, 0\n\tv_mbcnt_hi_u32_b32 %0, -1, %0" : "=v"(ln_));
;     if (b.w0 == 0 && ln_ == 0) {
;         unsigned* bar = b.bar; unsigned one_ = 1u;
;         asm volatile("" : "+s"(bar), "+v"(one_));
;         __builtin_amdgcn_s_waitcnt(0);
;         unsigned nloc = b.st[0], nx = b.st[1];
;         if (nloc == 0u) { xcd_barrier_complete(bar, b.x, nloc, nx); b.st[0] = nloc; b.st[1] = nx; }
;         const unsigned old = xb_add(&bar[XB_XSUB(b.x)], one_);
;         const unsigned gen = old / nloc;
;         if (old + 1u == (gen + 1u) * nloc) {
;             __builtin_amdgcn_fence(__ATOMIC_RELEASE, "agent");
;             asm volatile("s_waitcnt vmcnt(0)" ::: "memory");
;             const unsigned og = xb_add(&bar[XB_TOP], one_);
;             const unsigned tg = og / nx;
;             if (og + 1u == (tg + 1u) * nx) xb_add(&bar[XB_TOPGEN], one_);
;             else XB_SPIN(xb_ld(&bar[XB_TOPGEN]) == tg, bar);
;             __builtin_amdgcn_fence(__ATOMIC_ACQUIRE, "agent");
;             xb_add(&bar[XB_XGEN(b.x)], one_);
;             asm volatile("s_waitcnt vmcnt(0)" ::: "memory");
;         } else {
;             XB_SPIN(xb_ld(&bar[XB_XGEN(b.x)]) == gen, bar);
;             __builtin_amdgcn_fence(__ATOMIC_ACQUIRE, "agent");
;             asm volatile("s_waitcnt vmcnt(0)" ::: "memory");
;         }
;     }
;     __syncthreads();
.LBB0_142:
	s_lshl_b32 s2, s33, 8
	s_add_u32 s23, s34, s2
	s_addc_u32 s22, s35, 0
	v_mov_b32_e32 v1, s23
	v_add_co_u32_e32 v4, vcc, 0x1000, v1
	v_mov_b32_e32 v1, s22
	s_nop 0
	v_addc_co_u32_e32 v5, vcc, 0, v1, vcc
	flat_atomic_add v1, v[4:5], v10 offset:1024 sc0
	v_cvt_f32_u32_e32 v3, v2
	v_sub_u32_e32 v4, 0, v2
	v_rcp_iflag_f32_e32 v3, v3
	s_nop 0
	v_mul_f32_e32 v3, 0x4f7ffffe, v3
	v_cvt_u32_f32_e32 v3, v3
	v_mul_lo_u32 v4, v4, v3
	v_mul_hi_u32 v4, v3, v4
	v_add_u32_e32 v3, v3, v4
	s_waitcnt vmcnt(0) lgkmcnt(0)
	v_mul_hi_u32 v3, v1, v3
	v_mul_lo_u32 v5, v3, v2
	v_add_u32_e32 v4, 1, v1
	v_sub_u32_e32 v1, v1, v5
	v_add_u32_e32 v6, 1, v3
	v_cmp_ge_u32_e32 vcc, v1, v2
	v_sub_u32_e32 v5, v1, v2
	s_nop 0
	v_cndmask_b32_e32 v3, v3, v6, vcc
	v_cndmask_b32_e32 v1, v1, v5, vcc
	v_add_u32_e32 v5, 1, v3
	v_cmp_ge_u32_e32 vcc, v1, v2
	s_nop 1
	v_cndmask_b32_e32 v1, v3, v5, vcc
	v_mad_u64_u32 v[2:3], s[2:3], v2, v1, v[2:3]
	v_cmp_ne_u32_e32 vcc, v4, v2
	v_mov_b32_e32 v4, 0
	s_cbranch_vccnz .Lxbar0_poll
	buffer_wbl2 sc1
	s_waitcnt vmcnt(0)
	s_add_u32 s6, s23, 0x2400
	s_addc_u32 s7, s22, 0
	global_atomic_add v4, v10, s[6:7]
.Lxbar0_poll:
	buffer_inv sc1
	s_add_u32 s6, s34, 0x2400
	s_addc_u32 s7, s35, 0
	s_mov_b32 s2, 0
.Lxbar0_spin:
	global_load_dword v5, v4, s[6:7] sc1
	global_load_dword v6, v4, s[6:7] offset:256 sc1
	global_load_dword v7, v4, s[6:7] offset:512 sc1
	global_load_dword v8, v4, s[6:7] offset:768 sc1
	global_load_dword v9, v4, s[6:7] offset:1024 sc1
	global_load_dword v10, v4, s[6:7] offset:1280 sc1
	global_load_dword v11, v4, s[6:7] offset:1536 sc1
	global_load_dword v12, v4, s[6:7] offset:1792 sc1
	global_load_dword v13, v4, s[6:7] offset:2048 sc1
	global_load_dword v14, v4, s[6:7] offset:2304 sc1
	global_load_dword v15, v4, s[6:7] offset:2560 sc1
	global_load_dword v16, v4, s[6:7] offset:2816 sc1
	global_load_dword v17, v4, s[6:7] offset:3072 sc1
	global_load_dword v18, v4, s[6:7] offset:3328 sc1
	global_load_dword v19, v4, s[6:7] offset:3584 sc1
	global_load_dword v20, v4, s[6:7] offset:3840 sc1
	s_waitcnt vmcnt(0)
	v_sub_u32_e32 v5, v5, v1
	v_sub_u32_e32 v6, v6, v1
	v_sub_u32_e32 v7, v7, v1
	v_sub_u32_e32 v8, v8, v1
	v_sub_u32_e32 v9, v9, v1
	v_sub_u32_e32 v10, v10, v1
	v_sub_u32_e32 v11, v11, v1
	v_sub_u32_e32 v12, v12, v1
	v_sub_u32_e32 v13, v13, v1
	v_sub_u32_e32 v14, v14, v1
	v_sub_u32_e32 v15, v15, v1
	v_sub_u32_e32 v16, v16, v1
	v_sub_u32_e32 v17, v17, v1
	v_sub_u32_e32 v18, v18, v1
	v_sub_u32_e32 v19, v19, v1
	v_sub_u32_e32 v20, v20, v1
	v_med3_i32 v5, v5, 0, 1
	v_med3_i32 v6, v6, 0, 1
	v_med3_i32 v7, v7, 0, 1
	v_med3_i32 v8, v8, 0, 1
	v_med3_i32 v9, v9, 0, 1
	v_med3_i32 v10, v10, 0, 1
	v_med3_i32 v11, v11, 0, 1
	v_med3_i32 v12, v12, 0, 1
	v_med3_i32 v13, v13, 0, 1
	v_med3_i32 v14, v14, 0, 1
	v_med3_i32 v15, v15, 0, 1
	v_med3_i32 v16, v16, 0, 1
	v_med3_i32 v17, v17, 0, 1
	v_med3_i32 v18, v18, 0, 1
	v_med3_i32 v19, v19, 0, 1
	v_med3_i32 v20, v20, 0, 1
	v_add3_u32 v2, v5, v6, v7
	v_add3_u32 v2, v2, v8, v9
	v_add3_u32 v2, v2, v10, v11
	v_add3_u32 v2, v2, v12, v13
	v_add3_u32 v2, v2, v14, v15
	v_add3_u32 v2, v2, v16, v17
	v_add3_u32 v2, v2, v18, v19
	v_add_u32_e32 v2, v2, v20
	v_cmp_ge_u32_e32 vcc, v2, v0
	s_cbranch_vccnz .Lxbar0_done
	s_sleep 1
	s_add_i32 s2, s2, 1
	s_cmp_lt_u32 s2, 0x80000
	s_cbranch_scc1 .Lxbar0_spin
.Lxbar0_done:
.LBB0_172:
	s_or_b64 exec, exec, s[0:1]
	s_waitcnt lgkmcnt(0)
	s_barrier
; __device__ __forceinline__ unsigned xb_ld(unsigned* p)              { return __hip_atomic_load(p, __ATOMIC_RELAXED, __HIP_MEMORY_SCOPE_AGENT); }
; __device__ __forceinline__ void xcd_barrier_complete(unsigned* bar, unsigned x, unsigned& nloc, unsigned& nx) {
;     const unsigned G = gridDim.x * gridDim.y * gridDim.z;
;     unsigned sum, cnt, mine, sp = 0u;
;     for (;;) {
;         sum = 0u; cnt = 0u; mine = 0u;
; #pragma unroll
;         for (unsigned j = 0; j < 16; ++j) { const unsigned c = xb_ld(&bar[XB_XCNT(j)]); sum += c; cnt += (c > 0u) ? 1u : 0u; mine = (j == x) ? c : mine; }
;         if (sum == G) break;
;         __builtin_amdgcn_s_sleep(1);
;         if ((++sp & 255u) == 0u) { if (xb_ld(&bar[XB_TMO])) break; if (sp > XB_SPIN_CAP) { atomicAdd(&bar[XB_TMO], 1u); break; } }
;     }
;     nloc = mine > 0u ? mine : 1u; nx = cnt > 0u ? cnt : 1u;
; }
; __global__ void __launch_bounds__(512, 2) mega_fwd(Args args) {
;     ...
; #pragma unroll 1
;     for (int li = 0; li < DEPTH + (PROBE_COLD ? 1 : 0); ++li) {
;         const int l = li < DEPTH ? li : DEPTH - 1; const bool probe_ = li >= DEPTH;
;         const int pb = 1 + 10 * li;
;         const float lambda_init = (l == 0) ? 0.2f : 0.35550906759096927f;
.LBB0_173:
	s_and_b32 s0, s60, 0xffffffc0
	v_writelane_b32 v253, s0, 16
	s_mov_b32 s7, 0x20000
	v_readlane_b32 s2, v253, 0
	s_ashr_i32 s0, s2, 31
	s_lshr_b32 s0, s0, 29
	s_add_i32 s0, s2, s0
	s_ashr_i32 s0, s0, 3
	s_lshl_b32 s1, s2, 5
	s_mulk_i32 s0, 0xff01
	s_add_i32 s0, s0, s1
	v_writelane_b32 v253, s0, 17
	s_lshl_b32 s0, s2, 3
	v_readlane_b32 s3, v253, 7
	s_add_i32 s0, s3, s0
	v_writelane_b32 v253, s0, 18
	s_lshl_b32 s0, s2, 9
	s_lshl_b32 s77, s3, 4
	v_writelane_b32 v253, s0, 19
	s_add_i32 s1, s77, 0
	s_mul_i32 s0, s3, 0x3ff0
	s_add_i32 s2, s1, s0
	s_cmp_eq_u32 s61, 0
	v_writelane_b32 v253, s1, 20
	s_cselect_b64 s[0:1], -1, 0
	v_writelane_b32 v253, s0, 21
	s_mov_b32 s6, 0x1000000
	s_mov_b64 s[10:11], s[6:7]
	v_writelane_b32 v253, s1, 22
	v_mbcnt_lo_u32_b32 v0, -1, 0
	v_readlane_b32 s0, v253, 1
	v_readlane_b32 s1, v253, 2
	s_add_u32 s0, s0, 0xf0
	s_addc_u32 s1, s1, 0
	v_writelane_b32 v253, s0, 23
	s_cmp_eq_u32 s33, 15
	s_mov_b32 s31, 0
	v_writelane_b32 v253, s1, 24
	s_cselect_b64 s[0:1], -1, 0
	v_writelane_b32 v253, s0, 25
	s_cmp_eq_u32 s33, 14
	v_mov_b32_e32 v2, 0
	v_writelane_b32 v253, s1, 26
	s_cselect_b64 s[0:1], -1, 0
	v_writelane_b32 v253, s0, 27
	s_cmp_eq_u32 s33, 13
	v_mov_b32_e32 v210, 0x3727c5ac
	v_writelane_b32 v253, s1, 28
	s_cselect_b64 s[0:1], -1, 0
	v_writelane_b32 v253, s0, 29
	s_cmp_eq_u32 s33, 12
	v_mov_b32_e32 v211, 0x260
	v_writelane_b32 v253, s1, 30
	s_cselect_b64 s[0:1], -1, 0
	v_writelane_b32 v253, s0, 31
	s_cmp_eq_u32 s33, 11
	v_mov_b32_e32 v212, 0x358637bd
	v_writelane_b32 v253, s1, 32
	s_cselect_b64 s[0:1], -1, 0
	v_writelane_b32 v253, s0, 33
	s_cmp_eq_u32 s33, 10
	v_mov_b32_e32 v213, -1
	v_writelane_b32 v253, s1, 34
	s_cselect_b64 s[0:1], -1, 0
	v_writelane_b32 v253, s0, 35
	s_cmp_eq_u32 s33, 9
	v_mov_b32_e32 v214, 0x43e00000
	v_writelane_b32 v253, s1, 36
	s_cselect_b64 s[0:1], -1, 0
	v_writelane_b32 v253, s0, 37
	s_cmp_eq_u32 s33, 8
	v_mbcnt_hi_u32_b32 v215, -1, v0
	v_writelane_b32 v253, s1, 38
	s_cselect_b64 s[0:1], -1, 0
	v_writelane_b32 v253, s0, 39
	s_cmp_eq_u32 s33, 7
	v_mov_b32_e32 v216, 0xff800000
	v_writelane_b32 v253, s1, 40
	s_cselect_b64 s[0:1], -1, 0
	v_writelane_b32 v253, s0, 41
	s_cmp_eq_u32 s33, 6
	v_mov_b64_e32 v[250:251], 0x200
	v_writelane_b32 v253, s1, 42
	s_cselect_b64 s[0:1], -1, 0
	v_writelane_b32 v253, s0, 43
	s_cmp_eq_u32 s33, 5
	s_mov_b64 s[38:39], 0x80
	v_writelane_b32 v253, s1, 44
	s_cselect_b64 s[0:1], -1, 0
	v_writelane_b32 v253, s0, 45
	s_cmp_eq_u32 s33, 4
	s_mov_b32 s12, s31
	v_writelane_b32 v253, s1, 46
	s_cselect_b64 s[0:1], -1, 0
	v_writelane_b32 v253, s0, 47
	s_cmp_eq_u32 s33, 3
	s_nop 0
	v_writelane_b32 v253, s1, 48
	s_cselect_b64 s[0:1], -1, 0
	v_writelane_b32 v253, s0, 49
	s_cmp_eq_u32 s33, 2
	s_nop 0
	v_writelane_b32 v253, s1, 50
	s_cselect_b64 s[0:1], -1, 0
	v_writelane_b32 v253, s0, 51
	s_cmp_eq_u32 s33, 1
	s_nop 0
	v_writelane_b32 v253, s1, 52
	s_cselect_b64 s[0:1], -1, 0
	v_writelane_b32 v253, s0, 53
	s_cmp_eq_u32 s33, 0
	s_nop 0
	v_writelane_b32 v253, s1, 54
	s_cselect_b64 s[0:1], -1, 0
	v_writelane_b32 v253, s0, 55
	s_nop 1
	v_writelane_b32 v253, s1, 56
	s_lshl_b32 s0, s33, 6
	v_writelane_b32 v253, s0, 57
	s_lshl_b32 s0, s3, 2
	v_writelane_b32 v253, s0, 58
	s_add_i32 s0, s77, 0xffffff80
	v_writelane_b32 v253, s0, 59
	s_mul_i32 s0, s3, 0xffffca00
	v_writelane_b32 v253, s2, 60
	s_add_i32 s0, s2, s0
	v_writelane_b32 v253, s0, 61
	s_lshl_b32 s0, s3, 3
	v_writelane_b32 v253, s0, 62
	s_add_i32 s0, s3, 0x1e80
	v_writelane_b32 v253, s0, 63
	s_lshl_b32 s0, s3, 12
	v_writelane_b32 v254, s0, 0
	s_add_i32 s0, 0, 0x20040
	v_writelane_b32 v254, s0, 1
	s_add_i32 s0, 0, 0x20044
	v_writelane_b32 v254, s0, 2
	v_writelane_b32 v254, s8, 3
	s_mov_b32 s2, -1
	s_mov_b32 s3, s7
	v_writelane_b32 v254, s9, 4
	v_writelane_b32 v254, s10, 5
	v_writelane_b32 v254, s11, 6
	v_writelane_b32 v254, s0, 7
	s_mov_b32 s33, 0xc3e00000
	s_nop 0
	v_writelane_b32 v254, s1, 8
	v_writelane_b32 v254, s2, 9
	v_writelane_b32 v254, s3, 10
	s_add_i32 s0, 0, 0x1c800
	v_writelane_b32 v254, s0, 11
	s_add_i32 s0, 0, 0x10a00
	v_writelane_b32 v254, s0, 12
	s_add_i32 s0, 0, 0x20700
	v_writelane_b32 v254, s0, 13
	s_mov_b64 s[0:1], 0
	v_writelane_b32 v254, s0, 14
	s_nop 1
	v_writelane_b32 v254, s1, 15
	s_mov_b64 s[0:1], -1
	v_writelane_b32 v254, s0, 16
	s_nop 1
	v_writelane_b32 v254, s1, 17
	v_writelane_b32 v254, s77, 18
	s_branch .LBB0_177
.LBB0_175:
	s_or_b64 exec, exec, s[0:1]
	s_waitcnt lgkmcnt(0)
	s_barrier

; __device__ __forceinline__ unsigned xb_ld(unsigned* p)              { return __hip_atomic_load(p, __ATOMIC_RELAXED, __HIP_MEMORY_SCOPE_AGENT); }
; __device__ __forceinline__ unsigned xb_add(unsigned* p, unsigned v) { return __hip_atomic_fetch_add(p, v, __ATOMIC_RELAXED, __HIP_MEMORY_SCOPE_AGENT); }
; #define XB_SPIN(cond, bar) do { unsigned _sp = 0; while (cond) { __builtin_amdgcn_s_sleep(1); \
;     if ((++_sp & 255u) == 0u) { if (xb_ld(&(bar)[XB_TMO])) break; if (_sp > XB_SPIN_CAP) { atomicAdd(&(bar)[XB_TMO], 1u); break; } } } } while (0)
; __device__ __forceinline__ void xcd_barrier(const XcdBarrier& b) {
;     asm volatile("s_waitcnt vmcnt(0)" ::: "memory");
;     __syncthreads();
;     int ln_; asm volatile("v_mbcnt_lo_u32_b32 %0, -1, 0\n\tv_mbcnt_hi_u32_b32 %0, -1, %0" : "=v"(ln_));
;     if (b.w0 == 0 && ln_ == 0) {
;         unsigned* bar = b.bar; unsigned one_ = 1u;
;         asm volatile("" : "+s"(bar), "+v"(one_));
;         __builtin_amdgcn_s_waitcnt(0);
;         unsigned nloc = b.st[0], nx = b.st[1];
;         if (nloc == 0u) { xcd_barrier_complete(bar, b.x, nloc, nx); b.st[0] = nloc; b.st[1] = nx; }
;         const unsigned old = xb_add(&bar[XB_XSUB(b.x)], one_);
;         const unsigned gen = old / nloc;
;         if (old + 1u == (gen + 1u) * nloc) {
;             __builtin_amdgcn_fence(__ATOMIC_RELEASE, "agent");
;             asm volatile("s_waitcnt vmcnt(0)" ::: "memory");
;             const unsigned og = xb_add(&bar[XB_TOP], one_);
;             const unsigned tg = og / nx;
;             if (og + 1u == (tg + 1u) * nx) xb_add(&bar[XB_TOPGEN], one_);
;             else XB_SPIN(xb_ld(&bar[XB_TOPGEN]) == tg, bar);
;             __builtin_amdgcn_fence(__ATOMIC_ACQUIRE, "agent");
;             xb_add(&bar[XB_XGEN(b.x)], one_);
;             asm volatile("s_waitcnt vmcnt(0)" ::: "memory");
;         } else {
;             XB_SPIN(xb_ld(&bar[XB_XGEN(b.x)]) == gen, bar);
;             __builtin_amdgcn_fence(__ATOMIC_ACQUIRE, "agent");
;             asm volatile("s_waitcnt vmcnt(0)" ::: "memory");
;         }
;     }
;     __syncthreads();
.LBB0_430:
	v_readlane_b32 s4, v253, 57
	s_lshl_b32 s4, s4, 2
	s_add_u32 s25, s2, s4
	s_addc_u32 s24, s3, 0
	v_mov_b32_e32 v3, s25
	v_add_co_u32_e32 v6, vcc, 0x1000, v3
	v_mov_b32_e32 v3, s24
	s_nop 0
	v_addc_co_u32_e32 v7, vcc, 0, v3, vcc
	flat_atomic_add v5, v[6:7], v1 offset:1024 sc0
	v_cvt_f32_u32_e32 v3, v4
	v_sub_u32_e32 v6, 0, v4
	v_rcp_iflag_f32_e32 v3, v3
	s_nop 0
	v_mul_f32_e32 v3, 0x4f7ffffe, v3
	v_cvt_u32_f32_e32 v3, v3
	v_mul_lo_u32 v6, v6, v3
	v_mul_hi_u32 v6, v3, v6
	v_add_u32_e32 v3, v3, v6
	s_waitcnt vmcnt(0) lgkmcnt(0)
	v_mul_hi_u32 v3, v5, v3
	v_mul_lo_u32 v6, v3, v4
	v_sub_u32_e32 v6, v5, v6
	v_cmp_ge_u32_e32 vcc, v6, v4
	v_add_u32_e32 v7, 1, v3
	s_nop 0
	v_cndmask_b32_e32 v3, v3, v7, vcc
	v_sub_u32_e32 v7, v6, v4
	v_cndmask_b32_e32 v6, v6, v7, vcc
	v_cmp_ge_u32_e32 vcc, v6, v4
	v_add_u32_e32 v6, 1, v3
	s_nop 0
	v_cndmask_b32_e32 v3, v3, v6, vcc
	v_add_u32_e32 v6, 1, v5
	v_mad_u64_u32 v[4:5], s[4:5], v4, v3, v[4:5]
	v_cmp_ne_u32_e32 vcc, v6, v4
	v_mov_b32_e32 v4, 0
	s_cbranch_vccnz .Lxbar1_poll
	buffer_wbl2 sc1
	s_waitcnt vmcnt(0)
	s_add_u32 s8, s25, 0x2400
	s_addc_u32 s9, s24, 0
	global_atomic_add v4, v1, s[8:9]
.Lxbar1_poll:
	buffer_inv sc1
	s_add_u32 s8, s2, 0x2400
	s_addc_u32 s9, s3, 0
	s_mov_b32 s4, 0
.Lxbar1_spin:
	global_load_dword v5, v4, s[8:9] sc1
	global_load_dword v6, v4, s[8:9] offset:256 sc1
	global_load_dword v7, v4, s[8:9] offset:512 sc1
	global_load_dword v8, v4, s[8:9] offset:768 sc1
	global_load_dword v9, v4, s[8:9] offset:1024 sc1
	global_load_dword v10, v4, s[8:9] offset:1280 sc1
	global_load_dword v11, v4, s[8:9] offset:1536 sc1
	global_load_dword v12, v4, s[8:9] offset:1792 sc1
	global_load_dword v13, v4, s[8:9] offset:2048 sc1
	global_load_dword v14, v4, s[8:9] offset:2304 sc1
	global_load_dword v15, v4, s[8:9] offset:2560 sc1
	global_load_dword v16, v4, s[8:9] offset:2816 sc1
	global_load_dword v17, v4, s[8:9] offset:3072 sc1
	global_load_dword v18, v4, s[8:9] offset:3328 sc1
	global_load_dword v19, v4, s[8:9] offset:3584 sc1
	global_load_dword v20, v4, s[8:9] offset:3840 sc1
	s_waitcnt vmcnt(0)
	v_sub_u32_e32 v5, v5, v3
	v_sub_u32_e32 v6, v6, v3
	v_sub_u32_e32 v7, v7, v3
	v_sub_u32_e32 v8, v8, v3
	v_sub_u32_e32 v9, v9, v3
	v_sub_u32_e32 v10, v10, v3
	v_sub_u32_e32 v11, v11, v3
	v_sub_u32_e32 v12, v12, v3
	v_sub_u32_e32 v13, v13, v3
	v_sub_u32_e32 v14, v14, v3
	v_sub_u32_e32 v15, v15, v3
	v_sub_u32_e32 v16, v16, v3
	v_sub_u32_e32 v17, v17, v3
	v_sub_u32_e32 v18, v18, v3
	v_sub_u32_e32 v19, v19, v3
	v_sub_u32_e32 v20, v20, v3
	v_med3_i32 v5, v5, 0, 1
	v_med3_i32 v6, v6, 0, 1
	v_med3_i32 v7, v7, 0, 1
	v_med3_i32 v8, v8, 0, 1
	v_med3_i32 v9, v9, 0, 1
	v_med3_i32 v10, v10, 0, 1
	v_med3_i32 v11, v11, 0, 1
	v_med3_i32 v12, v12, 0, 1
	v_med3_i32 v13, v13, 0, 1
	v_med3_i32 v14, v14, 0, 1
	v_med3_i32 v15, v15, 0, 1
	v_med3_i32 v16, v16, 0, 1
	v_med3_i32 v17, v17, 0, 1
	v_med3_i32 v18, v18, 0, 1
	v_med3_i32 v19, v19, 0, 1
	v_med3_i32 v20, v20, 0, 1
	v_add3_u32 v1, v5, v6, v7
	v_add3_u32 v1, v1, v8, v9
	v_add3_u32 v1, v1, v10, v11
	v_add3_u32 v1, v1, v12, v13
	v_add3_u32 v1, v1, v14, v15
	v_add3_u32 v1, v1, v16, v17
	v_add3_u32 v1, v1, v18, v19
	v_add_u32_e32 v1, v1, v20
	v_cmp_ge_u32_e32 vcc, v1, v0
	s_cbranch_vccnz .Lxbar1_done
	s_sleep 1
	s_add_i32 s4, s4, 1
	s_cmp_lt_u32 s4, 0x80000
	s_cbranch_scc1 .Lxbar1_spin

; __device__ __forceinline__ unsigned xb_ld(unsigned* p)              { return __hip_atomic_load(p, __ATOMIC_RELAXED, __HIP_MEMORY_SCOPE_AGENT); }
; __device__ __forceinline__ unsigned xb_add(unsigned* p, unsigned v) { return __hip_atomic_fetch_add(p, v, __ATOMIC_RELAXED, __HIP_MEMORY_SCOPE_AGENT); }
; #define XB_SPIN(cond, bar) do { unsigned _sp = 0; while (cond) { __builtin_amdgcn_s_sleep(1); \
;     if ((++_sp & 255u) == 0u) { if (xb_ld(&(bar)[XB_TMO])) break; if (_sp > XB_SPIN_CAP) { atomicAdd(&(bar)[XB_TMO], 1u); break; } } } } while (0)
; __device__ __forceinline__ void xcd_barrier(const XcdBarrier& b) {
;     asm volatile("s_waitcnt vmcnt(0)" ::: "memory");
;     __syncthreads();
;     int ln_; asm volatile("v_mbcnt_lo_u32_b32 %0, -1, 0\n\tv_mbcnt_hi_u32_b32 %0, -1, %0" : "=v"(ln_));
;     if (b.w0 == 0 && ln_ == 0) {
;         unsigned* bar = b.bar; unsigned one_ = 1u;
;         asm volatile("" : "+s"(bar), "+v"(one_));
;         __builtin_amdgcn_s_waitcnt(0);
;         unsigned nloc = b.st[0], nx = b.st[1];
;         if (nloc == 0u) { xcd_barrier_complete(bar, b.x, nloc, nx); b.st[0] = nloc; b.st[1] = nx; }
;         const unsigned old = xb_add(&bar[XB_XSUB(b.x)], one_);
;         const unsigned gen = old / nloc;
;         if (old + 1u == (gen + 1u) * nloc) {
;             __builtin_amdgcn_fence(__ATOMIC_RELEASE, "agent");
;             asm volatile("s_waitcnt vmcnt(0)" ::: "memory");
;             const unsigned og = xb_add(&bar[XB_TOP], one_);
;             const unsigned tg = og / nx;
;             if (og + 1u == (tg + 1u) * nx) xb_add(&bar[XB_TOPGEN], one_);
;             else XB_SPIN(xb_ld(&bar[XB_TOPGEN]) == tg, bar);
;             __builtin_amdgcn_fence(__ATOMIC_ACQUIRE, "agent");
;             xb_add(&bar[XB_XGEN(b.x)], one_);
;             asm volatile("s_waitcnt vmcnt(0)" ::: "memory");
;         } else {
;             XB_SPIN(xb_ld(&bar[XB_XGEN(b.x)]) == gen, bar);
;             __builtin_amdgcn_fence(__ATOMIC_ACQUIRE, "agent");
;             asm volatile("s_waitcnt vmcnt(0)" ::: "memory");
;         }
;     }
;     __syncthreads();
.LBB0_681:
	v_readlane_b32 s6, v253, 57
	s_lshl_b32 s6, s6, 2
	s_add_u32 s27, s4, s6
	s_addc_u32 s26, s5, 0
	v_mov_b32_e32 v3, s27
	v_add_co_u32_e32 v6, vcc, 0x1000, v3
	v_mov_b32_e32 v3, s26
	s_nop 0
	v_addc_co_u32_e32 v7, vcc, 0, v3, vcc
	flat_atomic_add v5, v[6:7], v1 offset:1024 sc0
	v_cvt_f32_u32_e32 v3, v4
	v_sub_u32_e32 v6, 0, v4
	v_rcp_iflag_f32_e32 v3, v3
	s_nop 0
	v_mul_f32_e32 v3, 0x4f7ffffe, v3
	v_cvt_u32_f32_e32 v3, v3
	v_mul_lo_u32 v6, v6, v3
	v_mul_hi_u32 v6, v3, v6
	v_add_u32_e32 v3, v3, v6
	s_waitcnt vmcnt(0) lgkmcnt(0)
	v_mul_hi_u32 v3, v5, v3
	v_mul_lo_u32 v6, v3, v4
	v_sub_u32_e32 v6, v5, v6
	v_cmp_ge_u32_e32 vcc, v6, v4
	v_add_u32_e32 v7, 1, v3
	s_nop 0
	v_cndmask_b32_e32 v3, v3, v7, vcc
	v_sub_u32_e32 v7, v6, v4
	v_cndmask_b32_e32 v6, v6, v7, vcc
	v_cmp_ge_u32_e32 vcc, v6, v4
	v_add_u32_e32 v6, 1, v3
	s_nop 0
	v_cndmask_b32_e32 v3, v3, v6, vcc
	v_add_u32_e32 v6, 1, v5
	v_mad_u64_u32 v[4:5], s[6:7], v4, v3, v[4:5]
	v_cmp_ne_u32_e32 vcc, v6, v4
	v_mov_b32_e32 v4, 0
	s_cbranch_vccnz .Lxbar2_poll
	buffer_wbl2 sc1
	s_waitcnt vmcnt(0)
	s_add_u32 s10, s27, 0x2400
	s_addc_u32 s11, s26, 0
	global_atomic_add v4, v1, s[10:11]
.Lxbar2_poll:
	buffer_inv sc1
	s_add_u32 s10, s4, 0x2400
	s_addc_u32 s11, s5, 0
	s_mov_b32 s6, 0
.Lxbar2_spin:
	global_load_dword v5, v4, s[10:11] sc1
	global_load_dword v6, v4, s[10:11] offset:256 sc1
	global_load_dword v7, v4, s[10:11] offset:512 sc1
	global_load_dword v8, v4, s[10:11] offset:768 sc1
	global_load_dword v9, v4, s[10:11] offset:1024 sc1
	global_load_dword v10, v4, s[10:11] offset:1280 sc1
	global_load_dword v11, v4, s[10:11] offset:1536 sc1
	global_load_dword v12, v4, s[10:11] offset:1792 sc1
	global_load_dword v13, v4, s[10:11] offset:2048 sc1
	global_load_dword v14, v4, s[10:11] offset:2304 sc1
	global_load_dword v15, v4, s[10:11] offset:2560 sc1
	global_load_dword v16, v4, s[10:11] offset:2816 sc1
	global_load_dword v17, v4, s[10:11] offset:3072 sc1
	global_load_dword v18, v4, s[10:11] offset:3328 sc1
	global_load_dword v19, v4, s[10:11] offset:3584 sc1
	global_load_dword v20, v4, s[10:11] offset:3840 sc1
	s_waitcnt vmcnt(0)
	v_sub_u32_e32 v5, v5, v3
	v_sub_u32_e32 v6, v6, v3
	v_sub_u32_e32 v7, v7, v3
	v_sub_u32_e32 v8, v8, v3
	v_sub_u32_e32 v9, v9, v3
	v_sub_u32_e32 v10, v10, v3
	v_sub_u32_e32 v11, v11, v3
	v_sub_u32_e32 v12, v12, v3
	v_sub_u32_e32 v13, v13, v3
	v_sub_u32_e32 v14, v14, v3
	v_sub_u32_e32 v15, v15, v3
	v_sub_u32_e32 v16, v16, v3
	v_sub_u32_e32 v17, v17, v3
	v_sub_u32_e32 v18, v18, v3
	v_sub_u32_e32 v19, v19, v3
	v_sub_u32_e32 v20, v20, v3
	v_med3_i32 v5, v5, 0, 1
	v_med3_i32 v6, v6, 0, 1
	v_med3_i32 v7, v7, 0, 1
	v_med3_i32 v8, v8, 0, 1
	v_med3_i32 v9, v9, 0, 1
	v_med3_i32 v10, v10, 0, 1
	v_med3_i32 v11, v11, 0, 1
	v_med3_i32 v12, v12, 0, 1
	v_med3_i32 v13, v13, 0, 1
	v_med3_i32 v14, v14, 0, 1
	v_med3_i32 v15, v15, 0, 1
	v_med3_i32 v16, v16, 0, 1
	v_med3_i32 v17, v17, 0, 1
	v_med3_i32 v18, v18, 0, 1
	v_med3_i32 v19, v19, 0, 1
	v_med3_i32 v20, v20, 0, 1
	v_add3_u32 v1, v5, v6, v7
	v_add3_u32 v1, v1, v8, v9
	v_add3_u32 v1, v1, v10, v11
	v_add3_u32 v1, v1, v12, v13
	v_add3_u32 v1, v1, v14, v15
	v_add3_u32 v1, v1, v16, v17
	v_add3_u32 v1, v1, v18, v19
	v_add_u32_e32 v1, v1, v20
	v_cmp_ge_u32_e32 vcc, v1, v0
	s_cbranch_vccnz .Lxbar2_done
	s_sleep 1
	s_add_i32 s6, s6, 1
	s_cmp_lt_u32 s6, 0x80000
	s_cbranch_scc1 .Lxbar2_spin
.Lxbar2_done:
.LBB0_711:
	s_or_b64 exec, exec, s[2:3]
	s_waitcnt lgkmcnt(0)
	s_barrier

; __device__ __forceinline__ unsigned xb_ld(unsigned* p)              { return __hip_atomic_load(p, __ATOMIC_RELAXED, __HIP_MEMORY_SCOPE_AGENT); }
; __device__ __forceinline__ unsigned xb_add(unsigned* p, unsigned v) { return __hip_atomic_fetch_add(p, v, __ATOMIC_RELAXED, __HIP_MEMORY_SCOPE_AGENT); }
; #define XB_SPIN(cond, bar) do { unsigned _sp = 0; while (cond) { __builtin_amdgcn_s_sleep(1); \
;     if ((++_sp & 255u) == 0u) { if (xb_ld(&(bar)[XB_TMO])) break; if (_sp > XB_SPIN_CAP) { atomicAdd(&(bar)[XB_TMO], 1u); break; } } } } while (0)
; __device__ __forceinline__ void xcd_barrier(const XcdBarrier& b) {
;     ...
;         const unsigned old = xb_add(&bar[XB_XSUB(b.x)], one_);
;         const unsigned gen = old / nloc;
;         if (old + 1u == (gen + 1u) * nloc) {
;             __builtin_amdgcn_fence(__ATOMIC_RELEASE, "agent");
;             asm volatile("s_waitcnt vmcnt(0)" ::: "memory");
;             const unsigned og = xb_add(&bar[XB_TOP], one_);
;             const unsigned tg = og / nx;
;             if (og + 1u == (tg + 1u) * nx) xb_add(&bar[XB_TOPGEN], one_);
;             else XB_SPIN(xb_ld(&bar[XB_TOPGEN]) == tg, bar);
;             __builtin_amdgcn_fence(__ATOMIC_ACQUIRE, "agent");
;             xb_add(&bar[XB_XGEN(b.x)], one_);
.LBB0_928:
	v_readlane_b32 s6, v253, 57
	s_lshl_b32 s6, s6, 2
	s_add_u32 s29, s4, s6
	s_addc_u32 s28, s5, 0
	v_mov_b32_e32 v3, s29
	v_add_co_u32_e32 v6, vcc, 0x1000, v3
	v_mov_b32_e32 v3, s28
	s_nop 0
	v_addc_co_u32_e32 v7, vcc, 0, v3, vcc
	flat_atomic_add v5, v[6:7], v1 offset:1024 sc0
	v_cvt_f32_u32_e32 v3, v4
	v_sub_u32_e32 v6, 0, v4
	v_rcp_iflag_f32_e32 v3, v3
	s_nop 0
	v_mul_f32_e32 v3, 0x4f7ffffe, v3
	v_cvt_u32_f32_e32 v3, v3
	v_mul_lo_u32 v6, v6, v3
	v_mul_hi_u32 v6, v3, v6
	v_add_u32_e32 v3, v3, v6
	s_waitcnt vmcnt(0) lgkmcnt(0)
	v_mul_hi_u32 v3, v5, v3
	v_mul_lo_u32 v6, v3, v4
	v_sub_u32_e32 v6, v5, v6
	v_cmp_ge_u32_e32 vcc, v6, v4
	v_add_u32_e32 v7, 1, v3
	s_nop 0
	v_cndmask_b32_e32 v3, v3, v7, vcc
	v_sub_u32_e32 v7, v6, v4
	v_cndmask_b32_e32 v6, v6, v7, vcc
	v_cmp_ge_u32_e32 vcc, v6, v4
	v_add_u32_e32 v6, 1, v3
	s_nop 0
	v_cndmask_b32_e32 v3, v3, v6, vcc
	v_add_u32_e32 v6, 1, v5
	v_mad_u64_u32 v[4:5], s[6:7], v4, v3, v[4:5]
	v_cmp_ne_u32_e32 vcc, v6, v4
	v_mov_b32_e32 v4, 0
	s_cbranch_vccnz .Lxbar4_poll
	buffer_wbl2 sc1
	s_waitcnt vmcnt(0)
	s_add_u32 s10, s29, 0x2400
	s_addc_u32 s11, s28, 0
	global_atomic_add v4, v1, s[10:11]

; __device__ __forceinline__ unsigned xb_ld(unsigned* p)              { return __hip_atomic_load(p, __ATOMIC_RELAXED, __HIP_MEMORY_SCOPE_AGENT); }
; __device__ __forceinline__ unsigned xb_add(unsigned* p, unsigned v) { return __hip_atomic_fetch_add(p, v, __ATOMIC_RELAXED, __HIP_MEMORY_SCOPE_AGENT); }
; #define XB_SPIN(cond, bar) do { unsigned _sp = 0; while (cond) { __builtin_amdgcn_s_sleep(1); \
;     if ((++_sp & 255u) == 0u) { if (xb_ld(&(bar)[XB_TMO])) break; if (_sp > XB_SPIN_CAP) { atomicAdd(&(bar)[XB_TMO], 1u); break; } } } } while (0)
; __device__ __forceinline__ void xcd_barrier(const XcdBarrier& b) {
;     ...
;         const unsigned old = xb_add(&bar[XB_XSUB(b.x)], one_);
;         const unsigned gen = old / nloc;
;         if (old + 1u == (gen + 1u) * nloc) {
;             __builtin_amdgcn_fence(__ATOMIC_RELEASE, "agent");
;             asm volatile("s_waitcnt vmcnt(0)" ::: "memory");
;             const unsigned og = xb_add(&bar[XB_TOP], one_);
;             const unsigned tg = og / nx;
;             if (og + 1u == (tg + 1u) * nx) xb_add(&bar[XB_TOPGEN], one_);
;             else XB_SPIN(xb_ld(&bar[XB_TOPGEN]) == tg, bar);
;             __builtin_amdgcn_fence(__ATOMIC_ACQUIRE, "agent");
;             xb_add(&bar[XB_XGEN(b.x)], one_);
.LBB0_1016:
	v_readlane_b32 s4, v253, 57
	s_lshl_b32 s4, s4, 2
	s_add_u32 s27, s2, s4
	s_addc_u32 s26, s3, 0
	v_mov_b32_e32 v3, s27
	v_add_co_u32_e32 v6, vcc, 0x1000, v3
	v_mov_b32_e32 v3, s26
	s_nop 0
	v_addc_co_u32_e32 v7, vcc, 0, v3, vcc
	flat_atomic_add v5, v[6:7], v1 offset:1024 sc0
	v_cvt_f32_u32_e32 v3, v4
	v_sub_u32_e32 v6, 0, v4
	v_rcp_iflag_f32_e32 v3, v3
	s_nop 0
	v_mul_f32_e32 v3, 0x4f7ffffe, v3
	v_cvt_u32_f32_e32 v3, v3
	v_mul_lo_u32 v6, v6, v3
	v_mul_hi_u32 v6, v3, v6
	v_add_u32_e32 v3, v3, v6
	s_waitcnt vmcnt(0) lgkmcnt(0)
	v_mul_hi_u32 v3, v5, v3
	v_mul_lo_u32 v6, v3, v4
	v_sub_u32_e32 v6, v5, v6
	v_cmp_ge_u32_e32 vcc, v6, v4
	v_add_u32_e32 v7, 1, v3
	s_nop 0
	v_cndmask_b32_e32 v3, v3, v7, vcc
	v_sub_u32_e32 v7, v6, v4
	v_cndmask_b32_e32 v6, v6, v7, vcc
	v_cmp_ge_u32_e32 vcc, v6, v4
	v_add_u32_e32 v6, 1, v3
	s_nop 0
	v_cndmask_b32_e32 v3, v3, v6, vcc
	v_add_u32_e32 v6, 1, v5
	v_mad_u64_u32 v[4:5], s[4:5], v4, v3, v[4:5]
	v_cmp_ne_u32_e32 vcc, v6, v4
	v_mov_b32_e32 v4, 0
	s_cbranch_vccnz .Lxbar5_poll
	buffer_wbl2 sc1
	s_waitcnt vmcnt(0)
	s_add_u32 s8, s27, 0x2400
	s_addc_u32 s9, s26, 0
	global_atomic_add v4, v1, s[8:9]

; __device__ __forceinline__ unsigned xb_ld(unsigned* p)              { return __hip_atomic_load(p, __ATOMIC_RELAXED, __HIP_MEMORY_SCOPE_AGENT); }
; #define XB_SPIN(cond, bar) do { unsigned _sp = 0; while (cond) { __builtin_amdgcn_s_sleep(1); \
;     if ((++_sp & 255u) == 0u) { if (xb_ld(&(bar)[XB_TMO])) break; if (_sp > XB_SPIN_CAP) { atomicAdd(&(bar)[XB_TMO], 1u); break; } } } } while (0)
; __device__ __forceinline__ void xcd_barrier(const XcdBarrier& b) {
;     ...
;         } else {
;             XB_SPIN(xb_ld(&bar[XB_XGEN(b.x)]) == gen, bar);
;             __builtin_amdgcn_fence(__ATOMIC_ACQUIRE, "agent");
;             asm volatile("s_waitcnt vmcnt(0)" ::: "memory");
;         }
.Lxbar9_done:
	s_getpc_b64 s[98:99]
